# prefix scans in pool2 and front_kernel chunk sorts done with DPP (row_shr/row_bcast) instead of ds_bpermute ladders
# speedup vs baseline: 1.0176x; 1.0101x over previous
.LBB0_45:
	s_or_b64 exec, exec, s[8:9]
	v_mbcnt_lo_u32_b32 v53, -1, 0
	s_waitcnt lgkmcnt(0)
	s_barrier
	ds_read_b32 v69, v52
	v_and_b32_e32 v72, 63, v0
	s_waitcnt lgkmcnt(0)
	v_mov_b32_e32 v70, v69
	s_nop 1
	v_add_u32_dpp v70, v70, v70 row_shr:1 row_mask:0xf bank_mask:0xf bound_ctrl:1
	s_nop 1
	v_add_u32_dpp v70, v70, v70 row_shr:2 row_mask:0xf bank_mask:0xf bound_ctrl:1
	s_nop 1
	v_add_u32_dpp v70, v70, v70 row_shr:4 row_mask:0xf bank_mask:0xf bound_ctrl:1
	s_nop 1
	v_add_u32_dpp v70, v70, v70 row_shr:8 row_mask:0xf bank_mask:0xf bound_ctrl:1
	s_nop 1
	v_add_u32_dpp v70, v70, v70 row_bcast:15 row_mask:0xa bank_mask:0xf
	s_nop 1
	v_add_u32_dpp v70, v70, v70 row_bcast:31 row_mask:0xc bank_mask:0xf
	v_cmp_eq_u32_e64 s[8:9], 63, v72
	s_and_saveexec_b64 s[16:17], s[8:9]
	v_lshrrev_b32_e32 v53, 4, v0
	v_and_b32_e32 v53, 28, v53
	ds_write_b32 v53, v70 offset:2048
	s_or_b64 exec, exec, s[16:17]
	v_mov_b32_e32 v53, 0
	s_waitcnt lgkmcnt(0)
	s_barrier
	ds_read_b128 v[72:75], v53 offset:2048
	ds_read_b128 v[76:79], v53 offset:2064
	s_movk_i32 s8, 0x7f
	v_cmp_lt_u32_e64 s[8:9], s8, v0
	v_sub_u32_e32 v69, v70, v69
	s_waitcnt lgkmcnt(1)
	v_cndmask_b32_e64 v71, v72, 0, s[4:5]
	v_cndmask_b32_e64 v72, 0, v73, s[8:9]
	s_movk_i32 s8, 0xbf
	v_cmp_lt_u32_e64 s[8:9], s8, v0
	v_add3_u32 v69, v71, v69, v72
	s_nop 0
	v_cndmask_b32_e64 v73, 0, v74, s[8:9]
	s_movk_i32 s8, 0xff
	v_cmp_lt_u32_e64 s[8:9], s8, v0
	s_nop 1
	v_cndmask_b32_e64 v74, 0, v75, s[8:9]
	s_movk_i32 s8, 0x13f
	v_cmp_lt_u32_e64 s[8:9], s8, v0
	v_add3_u32 v69, v69, v73, v74
	s_waitcnt lgkmcnt(0)
	v_cndmask_b32_e64 v75, 0, v76, s[8:9]
	s_movk_i32 s8, 0x17f
	v_cmp_lt_u32_e64 s[8:9], s8, v0
	s_nop 1
	v_cndmask_b32_e64 v76, 0, v77, s[8:9]
	s_movk_i32 s8, 0x1bf
	v_cmp_lt_u32_e64 s[8:9], s8, v0
	v_add3_u32 v69, v69, v75, v76
	s_nop 0
	v_cndmask_b32_e64 v77, 0, v78, s[8:9]
	s_movk_i32 s8, 0x1ff
	v_cmp_lt_u32_e64 s[8:9], s8, v0
	s_nop 1
	v_cndmask_b32_e64 v78, 0, v79, s[8:9]
	s_movk_i32 s8, 0x188
	v_add3_u32 v69, v69, v77, v78
	v_cmp_gt_u32_e64 s[8:9], s8, v0
	ds_write_b32 v52, v69
	s_and_saveexec_b64 s[16:17], s[8:9]
	s_cbranch_execz .LBB0_49
	s_load_dwordx2 s[8:9], s[0:1], 0x80
	v_lshl_add_u32 v52, v0, 7, s3
	s_waitcnt lgkmcnt(0)
	v_lshl_add_u64 v[52:53], v[52:53], 2, s[8:9]
	global_store_dword v[52:53], v69, off

.LBB0_68:
	s_or_b64 exec, exec, s[8:9]
	v_mbcnt_lo_u32_b32 v69, -1, 0
	s_waitcnt lgkmcnt(0)
	s_barrier
	ds_read_b32 v68, v52
	v_and_b32_e32 v72, 63, v0
	s_waitcnt lgkmcnt(0)
	v_mov_b32_e32 v69, v68
	s_nop 1
	v_add_u32_dpp v69, v69, v69 row_shr:1 row_mask:0xf bank_mask:0xf bound_ctrl:1
	s_nop 1
	v_add_u32_dpp v69, v69, v69 row_shr:2 row_mask:0xf bank_mask:0xf bound_ctrl:1
	s_nop 1
	v_add_u32_dpp v69, v69, v69 row_shr:4 row_mask:0xf bank_mask:0xf bound_ctrl:1
	s_nop 1
	v_add_u32_dpp v69, v69, v69 row_shr:8 row_mask:0xf bank_mask:0xf bound_ctrl:1
	s_nop 1
	v_add_u32_dpp v69, v69, v69 row_bcast:15 row_mask:0xa bank_mask:0xf
	s_nop 1
	v_add_u32_dpp v69, v69, v69 row_bcast:31 row_mask:0xc bank_mask:0xf
	v_cmp_eq_u32_e64 s[8:9], 63, v72
	s_and_saveexec_b64 s[12:13], s[8:9]
	v_lshrrev_b32_e32 v70, 4, v0
	v_and_b32_e32 v70, 28, v70
	ds_write_b32 v70, v69 offset:2048
	s_or_b64 exec, exec, s[12:13]
	v_mov_b32_e32 v74, 0
	s_waitcnt lgkmcnt(0)
	s_barrier
	ds_read_b128 v[70:73], v74 offset:2048
	ds_read_b128 v[74:77], v74 offset:2064
	s_movk_i32 s3, 0x7f
	v_cmp_lt_u32_e64 s[8:9], s3, v0
	s_movk_i32 s3, 0xbf
	s_waitcnt lgkmcnt(1)
	v_cndmask_b32_e64 v70, v70, 0, s[4:5]
	v_cndmask_b32_e64 v71, 0, v71, s[8:9]
	v_cmp_lt_u32_e64 s[8:9], s3, v0
	s_movk_i32 s3, 0xff
	v_sub_u32_e32 v68, v69, v68
	v_cndmask_b32_e64 v72, 0, v72, s[8:9]
	v_cmp_lt_u32_e64 s[8:9], s3, v0
	s_movk_i32 s3, 0x13f
	v_add3_u32 v68, v70, v68, v71
	v_cndmask_b32_e64 v73, 0, v73, s[8:9]
	v_cmp_lt_u32_e64 s[8:9], s3, v0
	s_movk_i32 s3, 0x17f
	v_add3_u32 v68, v68, v72, v73
	s_waitcnt lgkmcnt(0)
	v_cndmask_b32_e64 v74, 0, v74, s[8:9]
	v_cmp_lt_u32_e64 s[8:9], s3, v0
	s_movk_i32 s3, 0x1bf
	s_nop 0
	v_cndmask_b32_e64 v75, 0, v75, s[8:9]
	v_cmp_lt_u32_e64 s[8:9], s3, v0
	s_movk_i32 s3, 0x1ff
	v_add3_u32 v68, v68, v74, v75
	v_cndmask_b32_e64 v76, 0, v76, s[8:9]
	v_cmp_lt_u32_e64 s[8:9], s3, v0
	s_movk_i32 s3, 0x188
	s_nop 0
	v_cndmask_b32_e64 v77, 0, v77, s[8:9]
	v_add3_u32 v68, v68, v76, v77
	v_cmp_gt_u32_e64 s[8:9], s3, v0
	ds_write_b32 v52, v68
	s_and_saveexec_b64 s[12:13], s[8:9]
	s_cbranch_execz .LBB0_72
	s_load_dwordx2 s[8:9], s[0:1], 0x78
	v_lshl_add_u32 v70, v0, 7, s2
	v_ashrrev_i32_e32 v71, 31, v70
	s_waitcnt lgkmcnt(0)
	v_lshl_add_u64 v[70:71], v[70:71], 2, s[8:9]
	global_store_dword v[70:71], v68, off

.LBB4_8:
	s_or_b64 exec, exec, s[0:1]
	v_mov_b32_e32 v70, 0x11020
	v_lshl_add_u32 v70, v74, 5, v70
	v_lshrrev_b32_e32 v93, 6, v94
	s_and_saveexec_b64 s[6:7], s[4:5]
	s_cbranch_execz .LBB4_12
	s_waitcnt vmcnt(0)
	v_add_u32_e32 v75, v95, v94
	v_lshl_add_u32 v75, v75, 2, v123
	ds_write_b32 v75, v96
	v_mov_b32_e32 v72, v71
	s_nop 1
	v_add_u32_dpp v72, v72, v72 row_shr:1 row_mask:0xf bank_mask:0xf bound_ctrl:1
	s_nop 1
	v_add_u32_dpp v72, v72, v72 row_shr:2 row_mask:0xf bank_mask:0xf bound_ctrl:1
	s_nop 1
	v_add_u32_dpp v72, v72, v72 row_shr:4 row_mask:0xf bank_mask:0xf bound_ctrl:1
	s_nop 1
	v_add_u32_dpp v72, v72, v72 row_shr:8 row_mask:0xf bank_mask:0xf bound_ctrl:1
	s_nop 1
	v_add_u32_dpp v72, v72, v72 row_bcast:15 row_mask:0xa bank_mask:0xf
	s_nop 1
	v_add_u32_dpp v72, v72, v72 row_bcast:31 row_mask:0xc bank_mask:0xf
	v_cmp_eq_u32_e64 s[0:1], 63, v92
	s_and_saveexec_b64 s[18:19], s[0:1]
	v_lshl_add_u32 v73, v93, 2, v70
	ds_write_b32 v73, v72
	s_or_b64 exec, exec, s[18:19]
